# plus: GQA QK^T K fragments read two rounds ahead (third fragment set), finish-softmax VALU spread over the QK^T gaps
# speedup vs baseline: 1.0095x; 1.0000x over previous
.LBB0_881:
	ds_read_b128 v[96:99], v216 offset:49152
	ds_read_b128 v[100:103], v216 offset:57344
	ds_read_b128 v[178:181], v218 offset:49152
	ds_read_b128 v[182:185], v218 offset:57344
	ds_read_b128 v[240:243], v219 offset:49152
	ds_read_b128 v[244:247], v219 offset:57344
	v_add_f32_e32 v88, v64, v65
	v_add_f32_e32 v89, v72, v73
	v_add_f32_e32 v90, v80, v81
	v_add_f32_e32 v91, v194, v195
	s_waitcnt lgkmcnt(5)
	v_mfma_f32_32x32x16_bf16 v[112:127], v[96:99], v[138:141], 0
	v_add_f32_e32 v88, v66, v88
	v_add_f32_e32 v89, v74, v89
	v_add_f32_e32 v90, v82, v90
	s_waitcnt lgkmcnt(4)
	v_mfma_f32_32x32x16_bf16 v[96:111], v[100:103], v[138:141], 0
	v_add_f32_e32 v91, v196, v91
	v_add_f32_e32 v88, v67, v88
	v_add_f32_e32 v89, v75, v89
	v_add_f32_e32 v90, v83, v90
	s_waitcnt lgkmcnt(3)
	v_mfma_f32_32x32x16_bf16 v[112:127], v[178:181], v[154:157], v[112:127]
	v_add_f32_e32 v91, v197, v91
	v_add_f32_e32 v88, v68, v88
	v_add_f32_e32 v89, v76, v89
	s_waitcnt lgkmcnt(2)
	v_mfma_f32_32x32x16_bf16 v[96:111], v[182:185], v[154:157], v[96:111]
	ds_read_b128 v[178:181], v220 offset:49152
	ds_read_b128 v[182:185], v220 offset:57344
	v_add_f32_e32 v90, v84, v90
	v_add_f32_e32 v91, v92, v91
	v_add_f32_e32 v88, v69, v88
	v_add_f32_e32 v89, v77, v89
	s_waitcnt lgkmcnt(3)
	v_mfma_f32_32x32x16_bf16 v[112:127], v[240:243], v[158:161], v[112:127]
	v_add_f32_e32 v90, v85, v90
	v_add_f32_e32 v91, v93, v91
	v_add_f32_e32 v88, v70, v88
	s_waitcnt lgkmcnt(2)
	v_mfma_f32_32x32x16_bf16 v[96:111], v[244:247], v[158:161], v[96:111]
	ds_read_b128 v[240:243], v221 offset:49152
	ds_read_b128 v[244:247], v221 offset:57344
	v_add_f32_e32 v89, v78, v89
	v_add_f32_e32 v90, v86, v90
	v_add_f32_e32 v91, v94, v91
	v_add_f32_e32 v88, v71, v88
	s_waitcnt lgkmcnt(3)
	v_mfma_f32_32x32x16_bf16 v[112:127], v[178:181], v[150:153], v[112:127]
	v_add_f32_e32 v89, v79, v89
	v_add_f32_e32 v90, v87, v90
	v_add_f32_e32 v91, v95, v91
	s_waitcnt lgkmcnt(2)
	v_mfma_f32_32x32x16_bf16 v[96:111], v[182:185], v[150:153], v[96:111]
	ds_read_b128 v[178:181], v222 offset:49152
	ds_read_b128 v[182:185], v222 offset:57344
	v_add_f32_e32 v88, v89, v88
	v_add_f32_e32 v89, v91, v90
	v_add_f32_e32 v227, v88, v89
	v_mov_b32_e32 v228, v227
	s_waitcnt lgkmcnt(3)
	v_mfma_f32_32x32x16_bf16 v[112:127], v[240:243], v[146:149], v[112:127]
	v_cvt_pk_bf16_f32 v88, v64, v65
	v_cvt_pk_bf16_f32 v89, v66, v67
	v_cvt_pk_bf16_f32 v90, v68, v69
	v_cvt_pk_bf16_f32 v91, v70, v71
	s_waitcnt lgkmcnt(2)
	v_mfma_f32_32x32x16_bf16 v[96:111], v[244:247], v[146:149], v[96:111]
	ds_read_b128 v[240:243], v224 offset:49152
	ds_read_b128 v[244:247], v224 offset:57344
	v_permlane32_swap_b32_e32 v227, v228
	v_permlane32_swap_b32_e32 v88, v90
	v_permlane32_swap_b32_e32 v89, v91
	s_waitcnt lgkmcnt(3)
	v_mfma_f32_32x32x16_bf16 v[112:127], v[178:181], v[142:145], v[112:127]
	v_cvt_pk_bf16_f32 v72, v72, v73
	v_cvt_pk_bf16_f32 v73, v74, v75
	v_cvt_pk_bf16_f32 v74, v76, v77
	v_cvt_pk_bf16_f32 v75, v78, v79
	s_waitcnt lgkmcnt(2)
	v_mfma_f32_32x32x16_bf16 v[96:111], v[182:185], v[142:145], v[96:111]
	ds_read_b128 v[178:181], v223 offset:49152
	ds_read_b128 v[182:185], v223 offset:57344
	v_cvt_pk_bf16_f32 v64, v80, v81
	v_cvt_pk_bf16_f32 v65, v82, v83
	v_cvt_pk_bf16_f32 v66, v84, v85
	s_waitcnt lgkmcnt(3)
	v_mfma_f32_32x32x16_bf16 v[112:127], v[240:243], v[134:137], v[112:127]
	v_cvt_pk_bf16_f32 v67, v86, v87
	v_cvt_pk_bf16_f32 v68, v194, v195
	v_cvt_pk_bf16_f32 v69, v196, v197
	v_cvt_pk_bf16_f32 v70, v92, v93
	s_waitcnt lgkmcnt(2)
	v_mfma_f32_32x32x16_bf16 v[96:111], v[244:247], v[134:137], v[96:111]
	v_cvt_pk_bf16_f32 v71, v94, v95
	v_permlane32_swap_b32_e32 v72, v74
	v_permlane32_swap_b32_e32 v73, v75
	s_waitcnt lgkmcnt(1)
	v_mfma_f32_32x32x16_bf16 v[112:127], v[178:181], v[130:133], v[112:127]
	v_permlane32_swap_b32_e32 v64, v66
	v_permlane32_swap_b32_e32 v65, v67
	v_permlane32_swap_b32_e32 v68, v70
	v_permlane32_swap_b32_e32 v69, v71
	s_waitcnt lgkmcnt(0)
	v_mfma_f32_32x32x16_bf16 v[96:111], v[182:185], v[130:133], v[96:111]
	s_add_i32 s2, s39, -1
	s_mul_i32 s2, s2, s62
	s_lshl_b32 s72, s2, 6
	s_lshl_b64 s[2:3], s[72:73], 1
	s_add_u32 s12, s10, s2
	s_addc_u32 s13, s11, s3
	s_add_u32 s2, s8, s2
	s_addc_u32 s3, s9, s3
	global_load_dwordx4 v[178:181], v128, s[12:13]
	global_load_dwordx4 v[182:185], v198, s[12:13]
	global_load_dwordx4 v[186:189], v128, s[2:3]
	global_load_dwordx4 v[190:193], v198, s[2:3]
	ds_read_b64_tr_b16 v[76:77], v209 offset:0
	ds_read_b64_tr_b16 v[78:79], v209 offset:0x800
	ds_read_b64_tr_b16 v[80:81], v209 offset:0x1000
	ds_read_b64_tr_b16 v[82:83], v209 offset:0x1800
	ds_read_b64_tr_b16 v[84:85], v209 offset:0x2000
	ds_read_b64_tr_b16 v[86:87], v209 offset:0x2800
	ds_read_b64_tr_b16 v[92:93], v209 offset:0x3000
	ds_read_b64_tr_b16 v[94:95], v209 offset:0x3800
	s_waitcnt lgkmcnt(0)
	s_nop 0
	v_mfma_f32_32x32x16_bf16 v[0:15], v[76:79], v[88:91], v[0:15]
	v_mfma_f32_32x32x16_bf16 v[0:15], v[80:83], v[72:75], v[0:15]
	v_mfma_f32_32x32x16_bf16 v[0:15], v[84:87], v[64:67], v[0:15]
	ds_read_b64_tr_b16 v[76:77], v209 offset:0x200
	ds_read_b64_tr_b16 v[78:79], v209 offset:0xa00
	ds_read_b64_tr_b16 v[80:81], v209 offset:0x1200
	v_mfma_f32_32x32x16_bf16 v[0:15], v[92:95], v[68:71], v[0:15]
	ds_read_b64_tr_b16 v[82:83], v209 offset:0x1a00
	ds_read_b64_tr_b16 v[84:85], v209 offset:0x2200
	ds_read_b64_tr_b16 v[86:87], v209 offset:0x2a00
	ds_read_b64_tr_b16 v[92:93], v209 offset:0x3200
	ds_read_b64_tr_b16 v[94:95], v209 offset:0x3a00
	s_waitcnt lgkmcnt(0)
	v_mfma_f32_32x32x16_bf16 v[48:63], v[76:79], v[88:91], v[48:63]
	v_mfma_f32_32x32x16_bf16 v[48:63], v[80:83], v[72:75], v[48:63]
	v_mfma_f32_32x32x16_bf16 v[48:63], v[84:87], v[64:67], v[48:63]
	ds_read_b64_tr_b16 v[76:77], v209 offset:0x400
	ds_read_b64_tr_b16 v[78:79], v209 offset:0xc00
	ds_read_b64_tr_b16 v[80:81], v209 offset:0x1400
	ds_read_b64_tr_b16 v[82:83], v209 offset:0x1c00
	v_mfma_f32_32x32x16_bf16 v[48:63], v[92:95], v[68:71], v[48:63]
	ds_read_b64_tr_b16 v[84:85], v209 offset:0x2400
	ds_read_b64_tr_b16 v[86:87], v209 offset:0x2c00
	ds_read_b64_tr_b16 v[92:93], v209 offset:0x3400
	ds_read_b64_tr_b16 v[94:95], v209 offset:0x3c00
	s_waitcnt lgkmcnt(0)
	v_mfma_f32_32x32x16_bf16 v[32:47], v[76:79], v[88:91], v[32:47]
	ds_read_b64_tr_b16 v[76:77], v209 offset:0x600
	ds_read_b64_tr_b16 v[78:79], v209 offset:0xe00
	v_exp_f32_e32 v234, v104
	v_exp_f32_e32 v235, v105
	v_exp_f32_e32 v236, v106
	v_exp_f32_e32 v237, v107
	v_exp_f32_e32 v238, v108
	v_exp_f32_e32 v239, v109
	v_exp_f32_e32 v231, v110
	v_exp_f32_e32 v249, v111
	v_mfma_f32_32x32x16_bf16 v[32:47], v[80:83], v[72:75], v[32:47]
	v_exp_f32_e32 v80, v112
	v_exp_f32_e32 v81, v113
	v_exp_f32_e32 v82, v114
	v_exp_f32_e32 v83, v115
	v_mfma_f32_32x32x16_bf16 v[32:47], v[84:87], v[64:67], v[32:47]
	v_exp_f32_e32 v84, v116
	v_exp_f32_e32 v85, v117
	v_exp_f32_e32 v86, v118
	v_exp_f32_e32 v87, v119
	v_exp_f32_e32 v112, v96
	v_exp_f32_e32 v113, v97
	v_exp_f32_e32 v114, v98
	v_exp_f32_e32 v115, v99
	v_exp_f32_e32 v116, v100
	v_exp_f32_e32 v117, v101
	v_exp_f32_e32 v118, v102
	v_exp_f32_e32 v119, v103
	v_mfma_f32_32x32x16_bf16 v[32:47], v[92:95], v[68:71], v[32:47]
	ds_read_b64_tr_b16 v[92:93], v209 offset:0x1600
	ds_read_b64_tr_b16 v[94:95], v209 offset:0x1e00
	ds_read_b64_tr_b16 v[96:97], v209 offset:0x2600
	ds_read_b64_tr_b16 v[98:99], v209 offset:0x2e00
	ds_read_b64_tr_b16 v[100:101], v209 offset:0x3600
	ds_read_b64_tr_b16 v[102:103], v209 offset:0x3e00
	s_waitcnt lgkmcnt(0)
	v_mfma_f32_32x32x16_bf16 v[16:31], v[76:79], v[88:91], v[16:31]
	v_exp_f32_e32 v88, v120
	v_exp_f32_e32 v89, v121
	v_exp_f32_e32 v90, v122
	v_exp_f32_e32 v91, v123
	v_mfma_f32_32x32x16_bf16 v[16:31], v[92:95], v[72:75], v[16:31]
	v_exp_f32_e32 v92, v124
	v_exp_f32_e32 v93, v125
	v_exp_f32_e32 v94, v126
	v_exp_f32_e32 v95, v127
	s_barrier
	v_mfma_f32_32x32x16_bf16 v[16:31], v[96:99], v[64:67], v[16:31]
	s_waitcnt vmcnt(4)
	s_waitcnt vmcnt(7)
	ds_write_b128 v212, v[162:165]
	s_waitcnt vmcnt(6)
	ds_write_b128 v213, v[166:169]
	s_waitcnt vmcnt(5)
	ds_write_b128 v214, v[170:173] offset:32768
	s_waitcnt vmcnt(4)
	ds_write_b128 v215, v[174:177] offset:32768
	v_mfma_f32_32x32x16_bf16 v[16:31], v[100:103], v[68:71], v[16:31]
.LBB0_883:
	s_waitcnt lgkmcnt(0)
	s_barrier
	ds_read_b128 v[64:67], v216 offset:32768
	ds_read_b128 v[68:71], v216 offset:40960
	ds_read_b128 v[162:165], v218 offset:32768
	ds_read_b128 v[166:169], v218 offset:40960
	ds_read_b128 v[240:243], v219 offset:32768
	ds_read_b128 v[244:247], v219 offset:40960
	v_add_f32_e32 v120, v80, v81
	v_add_f32_e32 v121, v88, v89
	v_add_f32_e32 v122, v112, v113
	v_add_f32_e32 v123, v234, v235
	s_waitcnt lgkmcnt(5)
	v_mfma_f32_32x32x16_bf16 v[96:111], v[64:67], v[138:141], 0
	v_add_f32_e32 v120, v82, v120
	v_add_f32_e32 v121, v90, v121
	v_add_f32_e32 v122, v114, v122
	s_waitcnt lgkmcnt(4)
	v_mfma_f32_32x32x16_bf16 v[64:79], v[68:71], v[138:141], 0
	v_add_f32_e32 v123, v236, v123
	v_add_f32_e32 v120, v83, v120
	v_add_f32_e32 v121, v91, v121
	v_add_f32_e32 v122, v115, v122
	s_waitcnt lgkmcnt(3)
	v_mfma_f32_32x32x16_bf16 v[96:111], v[162:165], v[154:157], v[96:111]
	v_add_f32_e32 v123, v237, v123
	v_add_f32_e32 v120, v84, v120
	v_add_f32_e32 v121, v92, v121
	s_waitcnt lgkmcnt(2)
	v_mfma_f32_32x32x16_bf16 v[64:79], v[166:169], v[154:157], v[64:79]
	ds_read_b128 v[162:165], v220 offset:32768
	ds_read_b128 v[166:169], v220 offset:40960
	v_add_f32_e32 v122, v116, v122
	v_add_f32_e32 v123, v238, v123
	v_add_f32_e32 v120, v85, v120
	v_add_f32_e32 v121, v93, v121
	s_waitcnt lgkmcnt(3)
	v_mfma_f32_32x32x16_bf16 v[96:111], v[240:243], v[158:161], v[96:111]
	v_add_f32_e32 v122, v117, v122
	v_add_f32_e32 v123, v239, v123
	v_add_f32_e32 v120, v86, v120
	s_waitcnt lgkmcnt(2)
	v_mfma_f32_32x32x16_bf16 v[64:79], v[244:247], v[158:161], v[64:79]
	ds_read_b128 v[240:243], v221 offset:32768
	ds_read_b128 v[244:247], v221 offset:40960
	v_add_f32_e32 v121, v94, v121
	v_add_f32_e32 v122, v118, v122
	v_add_f32_e32 v123, v231, v123
	v_add_f32_e32 v120, v87, v120
	s_waitcnt lgkmcnt(3)
	v_mfma_f32_32x32x16_bf16 v[96:111], v[162:165], v[150:153], v[96:111]
	v_add_f32_e32 v121, v95, v121
	v_add_f32_e32 v122, v119, v122
	v_add_f32_e32 v123, v249, v123
	s_waitcnt lgkmcnt(2)
	v_mfma_f32_32x32x16_bf16 v[64:79], v[166:169], v[150:153], v[64:79]
	ds_read_b128 v[162:165], v222 offset:32768
	ds_read_b128 v[166:169], v222 offset:40960
	v_add_f32_e32 v120, v121, v120
	v_add_f32_e32 v121, v123, v122
	v_add_f32_e32 v229, v120, v121
	v_mov_b32_e32 v233, v229
	s_waitcnt lgkmcnt(3)
	v_mfma_f32_32x32x16_bf16 v[96:111], v[240:243], v[146:149], v[96:111]
	v_permlane32_swap_b32_e32 v229, v233
	v_cvt_pk_bf16_f32 v124, v80, v81
	v_cvt_pk_bf16_f32 v125, v82, v83
	v_cvt_pk_bf16_f32 v126, v84, v85
	s_waitcnt lgkmcnt(2)
	v_mfma_f32_32x32x16_bf16 v[64:79], v[244:247], v[146:149], v[64:79]
	ds_read_b128 v[240:243], v224 offset:32768
	ds_read_b128 v[244:247], v224 offset:40960
	v_cvt_pk_bf16_f32 v127, v86, v87
	v_cvt_pk_bf16_f32 v120, v88, v89
	v_cvt_pk_bf16_f32 v121, v90, v91
	s_waitcnt lgkmcnt(3)
	v_mfma_f32_32x32x16_bf16 v[96:111], v[162:165], v[142:145], v[96:111]
	v_cvt_pk_bf16_f32 v122, v92, v93
	v_cvt_pk_bf16_f32 v123, v94, v95
	v_cvt_pk_bf16_f32 v112, v112, v113
	v_cvt_pk_bf16_f32 v113, v114, v115
	s_waitcnt lgkmcnt(2)
	v_mfma_f32_32x32x16_bf16 v[64:79], v[166:169], v[142:145], v[64:79]
	ds_read_b128 v[162:165], v223 offset:32768
	ds_read_b128 v[166:169], v223 offset:40960
	v_cvt_pk_bf16_f32 v114, v116, v117
	v_cvt_pk_bf16_f32 v115, v118, v119
	v_cvt_pk_bf16_f32 v116, v234, v235
	s_waitcnt lgkmcnt(3)
	v_mfma_f32_32x32x16_bf16 v[96:111], v[240:243], v[134:137], v[96:111]
	v_cvt_pk_bf16_f32 v117, v236, v237
	v_cvt_pk_bf16_f32 v118, v238, v239
	v_cvt_pk_bf16_f32 v119, v231, v249
	v_permlane32_swap_b32_e32 v124, v126
	s_waitcnt lgkmcnt(2)
	v_mfma_f32_32x32x16_bf16 v[64:79], v[244:247], v[134:137], v[64:79]
	v_permlane32_swap_b32_e32 v125, v127
	v_permlane32_swap_b32_e32 v120, v122
	v_permlane32_swap_b32_e32 v121, v123
	s_waitcnt lgkmcnt(1)
	v_mfma_f32_32x32x16_bf16 v[96:111], v[162:165], v[130:133], v[96:111]
	v_permlane32_swap_b32_e32 v112, v114
	v_permlane32_swap_b32_e32 v113, v115
	v_permlane32_swap_b32_e32 v116, v118
	v_permlane32_swap_b32_e32 v117, v119
	s_waitcnt lgkmcnt(0)
	v_mfma_f32_32x32x16_bf16 v[64:79], v[166:169], v[130:133], v[64:79]
	s_min_i32 s2, s39, s14
	s_mul_i32 s2, s2, s62
	s_lshl_b32 s72, s2, 6
	s_lshl_b64 s[2:3], s[72:73], 1
	s_add_u32 s12, s10, s2
	s_addc_u32 s13, s11, s3
	s_add_u32 s2, s8, s2
	s_addc_u32 s3, s9, s3
	global_load_dwordx4 v[162:165], v128, s[12:13]
	global_load_dwordx4 v[166:169], v198, s[12:13]
	global_load_dwordx4 v[170:173], v128, s[2:3]
	global_load_dwordx4 v[174:177], v198, s[2:3]
	ds_read_b64_tr_b16 v[80:81], v211 offset:0
	ds_read_b64_tr_b16 v[82:83], v211 offset:0x800
	ds_read_b64_tr_b16 v[84:85], v211 offset:0x1000
	ds_read_b64_tr_b16 v[86:87], v211 offset:0x1800
	ds_read_b64_tr_b16 v[88:89], v211 offset:0x2000
	ds_read_b64_tr_b16 v[90:91], v211 offset:0x2800
	ds_read_b64_tr_b16 v[92:93], v211 offset:0x3000
	ds_read_b64_tr_b16 v[94:95], v211 offset:0x3800
	s_waitcnt lgkmcnt(0)
	s_nop 0
	v_mfma_f32_32x32x16_bf16 v[0:15], v[80:83], v[124:127], v[0:15]
	v_mfma_f32_32x32x16_bf16 v[0:15], v[84:87], v[120:123], v[0:15]
	v_mfma_f32_32x32x16_bf16 v[0:15], v[88:91], v[112:115], v[0:15]
	ds_read_b64_tr_b16 v[80:81], v211 offset:0x200
	ds_read_b64_tr_b16 v[82:83], v211 offset:0xa00
	ds_read_b64_tr_b16 v[84:85], v211 offset:0x1200
	v_mfma_f32_32x32x16_bf16 v[0:15], v[92:95], v[116:119], v[0:15]
	ds_read_b64_tr_b16 v[86:87], v211 offset:0x1a00
	ds_read_b64_tr_b16 v[88:89], v211 offset:0x2200
	ds_read_b64_tr_b16 v[90:91], v211 offset:0x2a00
	ds_read_b64_tr_b16 v[92:93], v211 offset:0x3200
	ds_read_b64_tr_b16 v[94:95], v211 offset:0x3a00
	s_waitcnt lgkmcnt(0)
	v_mfma_f32_32x32x16_bf16 v[48:63], v[80:83], v[124:127], v[48:63]
	v_mfma_f32_32x32x16_bf16 v[48:63], v[84:87], v[120:123], v[48:63]
	v_mfma_f32_32x32x16_bf16 v[48:63], v[88:91], v[112:115], v[48:63]
	ds_read_b64_tr_b16 v[80:81], v211 offset:0x400
	ds_read_b64_tr_b16 v[82:83], v211 offset:0xc00
	ds_read_b64_tr_b16 v[84:85], v211 offset:0x1400
	ds_read_b64_tr_b16 v[86:87], v211 offset:0x1c00
	v_mfma_f32_32x32x16_bf16 v[48:63], v[92:95], v[116:119], v[48:63]
	ds_read_b64_tr_b16 v[88:89], v211 offset:0x2400
	ds_read_b64_tr_b16 v[90:91], v211 offset:0x2c00
	ds_read_b64_tr_b16 v[92:93], v211 offset:0x3400
	ds_read_b64_tr_b16 v[94:95], v211 offset:0x3c00
	s_waitcnt lgkmcnt(0)
	v_mfma_f32_32x32x16_bf16 v[32:47], v[80:83], v[124:127], v[32:47]
	v_exp_f32_e32 v80, v64
	v_exp_f32_e32 v81, v65
	v_exp_f32_e32 v64, v96
	v_exp_f32_e32 v65, v97
	v_exp_f32_e32 v82, v66
	v_exp_f32_e32 v83, v67
	v_exp_f32_e32 v66, v98
	v_exp_f32_e32 v67, v99
	v_mfma_f32_32x32x16_bf16 v[32:47], v[84:87], v[120:123], v[32:47]
	v_exp_f32_e32 v84, v68
	v_exp_f32_e32 v85, v69
	v_exp_f32_e32 v68, v100
	v_exp_f32_e32 v69, v101
	v_exp_f32_e32 v86, v70
	v_exp_f32_e32 v87, v71
	v_exp_f32_e32 v70, v102
	v_exp_f32_e32 v71, v103
	v_mfma_f32_32x32x16_bf16 v[32:47], v[88:91], v[112:115], v[32:47]
	v_exp_f32_e32 v194, v72
	v_exp_f32_e32 v195, v73
	ds_read_b64_tr_b16 v[72:73], v211 offset:0x600
	v_exp_f32_e32 v196, v74
	v_exp_f32_e32 v197, v75
	ds_read_b64_tr_b16 v[74:75], v211 offset:0xe00
	v_mfma_f32_32x32x16_bf16 v[32:47], v[92:95], v[116:119], v[32:47]
	v_exp_f32_e32 v92, v76
	v_exp_f32_e32 v93, v77
	ds_read_b64_tr_b16 v[76:77], v211 offset:0x1600
	v_exp_f32_e32 v94, v78
	v_exp_f32_e32 v95, v79
	ds_read_b64_tr_b16 v[78:79], v211 offset:0x1e00
	ds_read_b64_tr_b16 v[96:97], v211 offset:0x2600
	ds_read_b64_tr_b16 v[98:99], v211 offset:0x2e00
	ds_read_b64_tr_b16 v[100:101], v211 offset:0x3600
	ds_read_b64_tr_b16 v[102:103], v211 offset:0x3e00
	s_waitcnt lgkmcnt(0)
	v_mfma_f32_32x32x16_bf16 v[16:31], v[72:75], v[124:127], v[16:31]
	v_exp_f32_e32 v72, v104
	v_exp_f32_e32 v73, v105
	v_exp_f32_e32 v74, v106
	v_exp_f32_e32 v75, v107
	v_mfma_f32_32x32x16_bf16 v[16:31], v[76:79], v[120:123], v[16:31]
	v_exp_f32_e32 v76, v108
	v_exp_f32_e32 v77, v109
	v_exp_f32_e32 v78, v110
	v_exp_f32_e32 v79, v111
	s_barrier
	v_mfma_f32_32x32x16_bf16 v[16:31], v[96:99], v[112:115], v[16:31]
	s_waitcnt vmcnt(4)
	s_waitcnt vmcnt(7)
	ds_write_b128 v212, v[178:181] offset:16384
	s_waitcnt vmcnt(6)
	ds_write_b128 v213, v[182:185] offset:16384
	s_waitcnt vmcnt(5)
	ds_write_b128 v214, v[186:189] offset:49152
	s_waitcnt vmcnt(4)
	ds_write_b128 v215, v[190:193] offset:49152
	v_mfma_f32_32x32x16_bf16 v[16:31], v[100:103], v[116:119], v[16:31]
